# P6 ln_router: the eight modulation-vector loads of a batch change issued back to back with counted waits (were three serialised waits)
# speedup vs baseline: 1.0030x; 1.0030x over previous
.LBB0_984:
	s_min_i32 s12, s12, 0x1000
	s_ashr_i32 s12, s12, 9
	s_cmp_eq_u32 s12, s50
	s_cbranch_scc1 .LBB0_986
	s_mul_i32 s34, s12, 6
	s_ashr_i32 s35, s34, 31
	s_lshl_b64 s[34:35], s[34:35], 12
	s_add_u32 s13, s44, s34
	s_addc_u32 s37, s45, s35
	s_add_u32 s34, s13, 0x3000
	s_addc_u32 s35, s37, 0
	s_add_u32 s36, s13, 0x4000
	s_addc_u32 s37, s37, 0
	v_lshl_add_u64 v[98:99], s[36:37], 0, v[194:195]
	v_lshl_add_u64 v[118:119], s[34:35], 0, v[194:195]
	v_lshl_add_u64 v[154:155], s[36:37], 0, v[196:197]
	v_lshl_add_u64 v[158:159], s[34:35], 0, v[196:197]
	global_load_dwordx4 v[98:101], v[98:99], off
	s_mov_b32 s50, s12
	global_load_dwordx4 v[118:121], v[118:119], off
	global_load_dwordx4 v[138:141], v[154:155], off offset:1024
	global_load_dwordx4 v[142:145], v[158:159], off offset:1024
	global_load_dwordx4 v[146:149], v[154:155], off offset:2048
	global_load_dwordx4 v[216:219], v[158:159], off offset:2048
	global_load_dwordx4 v[154:157], v[154:155], off offset:3072
	global_load_dwordx4 v[158:161], v[158:159], off offset:3072
	s_waitcnt vmcnt(7)
	v_pk_add_f32 v[100:101], v[100:101], 1.0 op_sel_hi:[1,0]
	v_pk_add_f32 v[98:99], v[98:99], 1.0 op_sel_hi:[1,0]
	s_waitcnt vmcnt(5)
	v_pk_add_f32 v[140:141], v[140:141], 1.0 op_sel_hi:[1,0]
	v_pk_add_f32 v[138:139], v[138:139], 1.0 op_sel_hi:[1,0]
	s_waitcnt vmcnt(3)
	v_pk_add_f32 v[152:153], v[148:149], 1.0 op_sel_hi:[1,0]
	v_pk_add_f32 v[150:151], v[146:147], 1.0 op_sel_hi:[1,0]
	s_waitcnt vmcnt(2)
	v_mov_b32_e32 v146, v216
	v_mov_b32_e32 v147, v217
	v_mov_b32_e32 v148, v218
	v_mov_b32_e32 v149, v219
	s_waitcnt vmcnt(1)
	v_pk_add_f32 v[156:157], v[156:157], 1.0 op_sel_hi:[1,0]
	v_pk_add_f32 v[154:155], v[154:155], 1.0 op_sel_hi:[1,0]
